# speedup vs baseline: 1.0081x; 1.0029x over previous
.Lu0_1:
	ds_read_b64_tr_b16 v[178:179], v206 offset:24576
	ds_read_b64_tr_b16 v[180:181], v206 offset:25600
	s_waitcnt lgkmcnt(9)
	v_mfma_f32_32x32x16_f16 v[98:113], v[82:85], v[154:157], v[34:49]
	v_add_f32_e32 v224, v66, v68
	v_add_f32_e32 v225, v67, v69
	v_add_f32_e32 v224, v70, v224
	v_add_f32_e32 v225, v71, v225
	v_cvt_pk_f16_f32 v158, v66, v67
	v_cvt_pk_f16_f32 v159, v68, v69
	ds_read_b64_tr_b16 v[174:175], v207 offset:24576
	ds_read_b64_tr_b16 v[176:177], v207 offset:25600
	s_waitcnt lgkmcnt(10)
	v_mfma_f32_32x32x16_f16 v[82:97], v[170:173], v[154:157], v[34:49]
	v_add_f32_e32 v224, v72, v224
	v_add_f32_e32 v225, v73, v225
	v_add_f32_e32 v224, v74, v224
	v_add_f32_e32 v225, v75, v225
	v_cvt_pk_f16_f32 v160, v70, v71
	v_cvt_pk_f16_f32 v161, v72, v73
	ds_read_b64_tr_b16 v[170:171], v206 offset:26624
	ds_read_b64_tr_b16 v[172:173], v206 offset:27648
	s_waitcnt lgkmcnt(11)
	v_mfma_f32_32x32x16_f16 v[98:113], v[166:169], v[146:149], v[98:113]
	v_add_f32_e32 v224, v76, v224
	v_add_f32_e32 v225, v77, v225
	v_add_f32_e32 v224, v78, v224
	v_add_f32_e32 v225, v79, v225
	v_cvt_pk_f16_f32 v150, v74, v75
	v_cvt_pk_f16_f32 v151, v76, v77
	ds_read_b64_tr_b16 v[74:75], v207 offset:26624
	ds_read_b64_tr_b16 v[76:77], v207 offset:27648
	s_waitcnt lgkmcnt(12)
	v_mfma_f32_32x32x16_f16 v[82:97], v[162:165], v[146:149], v[82:97]
	v_add_f32_e32 v224, v80, v224
	v_add_f32_e32 v225, v81, v225
	v_add_f32_e32 v224, v50, v224
	v_add_f32_e32 v225, v51, v225
	v_cvt_pk_f16_f32 v152, v78, v79
	v_cvt_pk_f16_f32 v153, v80, v81
	ds_read_b64_tr_b16 v[70:71], v206 offset:28672
	ds_read_b64_tr_b16 v[72:73], v206 offset:29696
	s_waitcnt lgkmcnt(13)
	v_mfma_f32_32x32x16_f16 v[98:113], v[126:129], v[138:141], v[98:113]
	v_add_f32_e32 v224, v52, v224
	v_add_f32_e32 v225, v53, v225
	v_add_f32_e32 v224, v54, v224
	v_add_f32_e32 v225, v55, v225
	v_cvt_pk_f16_f32 v142, v50, v51
	v_cvt_pk_f16_f32 v143, v52, v53
	ds_read_b64_tr_b16 v[66:67], v207 offset:28672
	ds_read_b64_tr_b16 v[68:69], v207 offset:29696
	s_waitcnt lgkmcnt(14)
	v_mfma_f32_32x32x16_f16 v[82:97], v[122:125], v[138:141], v[82:97]
	v_add_f32_e32 v224, v56, v224
	v_add_f32_e32 v225, v57, v225
	v_add_f32_e32 v224, v58, v224
	v_add_f32_e32 v225, v59, v225
	v_cvt_pk_f16_f32 v144, v54, v55
	v_cvt_pk_f16_f32 v145, v56, v57
	ds_read_b64_tr_b16 v[54:55], v206 offset:30720
	ds_read_b64_tr_b16 v[56:57], v206 offset:31744
	s_waitcnt lgkmcnt(14)
	v_mfma_f32_32x32x16_f16 v[98:113], v[118:121], v[134:137], v[98:113]
	v_add_f32_e32 v224, v60, v224
	v_add_f32_e32 v225, v61, v225
	v_add_f32_e32 v224, v62, v224
	v_add_f32_e32 v225, v63, v225
	v_cvt_pk_f16_f32 v130, v58, v59
	v_cvt_pk_f16_f32 v131, v60, v61
	ds_read_b64_tr_b16 v[50:51], v207 offset:30720
	ds_read_b64_tr_b16 v[52:53], v207 offset:31744
	v_mfma_f32_32x32x16_f16 v[82:97], v[114:117], v[134:137], v[82:97]
	v_add_f32_e32 v224, v64, v224
	v_add_f32_e32 v225, v65, v225
	v_add_f32_e32 v60, v224, v225
	v_cvt_pk_f16_f32 v132, v62, v63
	v_cvt_pk_f16_f32 v133, v64, v65
	s_add_i32 s26, s42, s36
	s_mov_b32 m0, s26
	s_nop 0
	global_load_lds_dwordx4 v221, s[50:51]
	s_add_i32 s26, s39, s35
	s_mov_b32 m0, s26
	s_nop 0
	global_load_lds_dwordx4 v222, s[52:53]
	v_max_f32_e32 v58, v98, v99
	v_max3_f32 v59, v100, v101, v83
	v_max3_f32 v58, v58, v82, v84
	v_max3_f32 v58, v58, v85, v102
	v_max3_f32 v59, v59, v104, v105
	v_max3_f32 v58, v58, v103, v86
	v_max3_f32 v59, v59, v88, v89
	v_max3_f32 v58, v58, v87, v106
	v_max3_f32 v59, v59, v108, v109
	v_max3_f32 v58, v58, v107, v90
	v_max3_f32 v59, v59, v92, v93
	v_max3_f32 v58, v58, v91, v110
	v_max3_f32 v59, v59, v112, v113
	v_max3_f32 v58, v58, v111, v94
	v_max3_f32 v59, v59, v96, v97
	v_max3_f32 v58, v58, v95, v59
	v_add_f32_e32 v198, v183, v60
	v_cmp_lt_f32_e32 vcc, s41, v58
	s_cmp_lg_u64 vcc, 0
	s_cselect_b64 s[26:27], -1, 0
	s_cbranch_vccnz .Lu0_9

.Lu0_4:
	s_add_i32 s26, s39, 0x2000
	s_cmpk_lg_i32 s39, 0x4000
	s_cselect_b32 s43, s26, 0
	ds_read_b64_tr_b16 v[126:127], v206 offset:32768
	ds_read_b64_tr_b16 v[128:129], v206 offset:33792
	s_waitcnt lgkmcnt(9)
	v_mfma_f32_32x32x16_f16 v[66:81], v[58:61], v[154:157], v[34:49]
	v_add_f32_e32 v224, v98, v100
	v_add_f32_e32 v225, v99, v101
	v_add_f32_e32 v224, v102, v224
	v_add_f32_e32 v225, v103, v225
	v_cvt_pk_f16_f32 v158, v98, v99
	v_cvt_pk_f16_f32 v159, v100, v101
	ds_read_b64_tr_b16 v[122:123], v207 offset:32768
	ds_read_b64_tr_b16 v[124:125], v207 offset:33792
	s_waitcnt lgkmcnt(10)
	v_mfma_f32_32x32x16_f16 v[50:65], v[114:117], v[154:157], v[34:49]
	v_add_f32_e32 v224, v104, v224
	v_add_f32_e32 v225, v105, v225
	v_add_f32_e32 v224, v106, v224
	v_add_f32_e32 v225, v107, v225
	v_cvt_pk_f16_f32 v160, v102, v103
	v_cvt_pk_f16_f32 v161, v104, v105
	ds_read_b64_tr_b16 v[118:119], v206 offset:34816
	ds_read_b64_tr_b16 v[120:121], v206 offset:35840
	s_waitcnt lgkmcnt(11)
	v_mfma_f32_32x32x16_f16 v[66:81], v[182:185], v[146:149], v[66:81]
	v_add_f32_e32 v224, v108, v224
	v_add_f32_e32 v225, v109, v225
	v_add_f32_e32 v224, v110, v224
	v_add_f32_e32 v225, v111, v225
	v_cvt_pk_f16_f32 v150, v106, v107
	v_cvt_pk_f16_f32 v151, v108, v109
	ds_read_b64_tr_b16 v[114:115], v207 offset:34816
	ds_read_b64_tr_b16 v[116:117], v207 offset:35840
	s_waitcnt lgkmcnt(12)
	v_mfma_f32_32x32x16_f16 v[50:65], v[174:177], v[146:149], v[50:65]
	v_add_f32_e32 v224, v112, v224
	v_add_f32_e32 v225, v113, v225
	v_add_f32_e32 v224, v82, v224
	v_add_f32_e32 v225, v83, v225
	v_cvt_pk_f16_f32 v152, v110, v111
	v_cvt_pk_f16_f32 v153, v112, v113
	ds_read_b64_tr_b16 v[106:107], v206 offset:36864
	ds_read_b64_tr_b16 v[108:109], v206 offset:37888
	s_waitcnt lgkmcnt(13)
	v_mfma_f32_32x32x16_f16 v[66:81], v[178:181], v[138:141], v[66:81]
	v_add_f32_e32 v224, v84, v224
	v_add_f32_e32 v225, v85, v225
	v_add_f32_e32 v224, v86, v224
	v_add_f32_e32 v225, v87, v225
	v_cvt_pk_f16_f32 v142, v82, v83
	v_cvt_pk_f16_f32 v143, v84, v85
	ds_read_b64_tr_b16 v[102:103], v207 offset:36864
	ds_read_b64_tr_b16 v[104:105], v207 offset:37888
	s_waitcnt lgkmcnt(14)
	v_mfma_f32_32x32x16_f16 v[50:65], v[166:169], v[138:141], v[50:65]
	v_add_f32_e32 v224, v88, v224
	v_add_f32_e32 v225, v89, v225
	v_add_f32_e32 v224, v90, v224
	v_add_f32_e32 v225, v91, v225
	v_cvt_pk_f16_f32 v144, v86, v87
	v_cvt_pk_f16_f32 v145, v88, v89
	ds_read_b64_tr_b16 v[98:99], v206 offset:38912
	ds_read_b64_tr_b16 v[100:101], v206 offset:39936
	s_waitcnt lgkmcnt(14)
	v_mfma_f32_32x32x16_f16 v[66:81], v[170:173], v[134:137], v[66:81]
	v_add_f32_e32 v224, v92, v224
	v_add_f32_e32 v225, v93, v225
	v_add_f32_e32 v224, v94, v224
	v_add_f32_e32 v225, v95, v225
	v_cvt_pk_f16_f32 v130, v90, v91
	v_cvt_pk_f16_f32 v131, v92, v93
	ds_read_b64_tr_b16 v[86:87], v207 offset:38912
	ds_read_b64_tr_b16 v[88:89], v207 offset:39936
	v_mfma_f32_32x32x16_f16 v[50:65], v[162:165], v[134:137], v[50:65]
	v_add_f32_e32 v224, v96, v224
	v_add_f32_e32 v225, v97, v225
	v_add_f32_e32 v84, v224, v225
	v_cvt_pk_f16_f32 v132, v94, v95
	v_cvt_pk_f16_f32 v133, v96, v97
	s_add_u32 s54, s50, 0x2000
	s_addc_u32 s55, s51, 0
	s_add_i32 s26, s39, s36
	s_mov_b32 m0, s26
	s_nop 0
	global_load_lds_dwordx4 v221, s[54:55]
	v_max_f32_e32 v82, v66, v67
	s_nop 1
	v_max3_f32 v83, v68, v69, v51
	v_max3_f32 v82, v82, v50, v52
	v_max3_f32 v82, v82, v53, v70
	v_max3_f32 v83, v83, v72, v73
	v_max3_f32 v82, v82, v71, v54
	v_max3_f32 v83, v83, v56, v57
	v_max3_f32 v82, v82, v55, v74
	v_max3_f32 v83, v83, v76, v77
	v_max3_f32 v82, v82, v75, v58
	v_max3_f32 v83, v83, v60, v61
	v_max3_f32 v82, v82, v59, v78
	v_max3_f32 v83, v83, v80, v81
	v_max3_f32 v82, v82, v79, v62
	v_max3_f32 v83, v83, v64, v65
	v_max3_f32 v82, v82, v63, v83
	v_add_f32_e32 v183, v198, v84
	s_add_u32 s54, s52, 0x2000
	s_addc_u32 s55, s53, 0
	s_add_i32 s26, s43, s35
	s_mov_b32 m0, s26
	s_nop 0
	global_load_lds_dwordx4 v222, s[54:55]
	v_cmp_lt_f32_e32 vcc, s41, v82
	s_cmp_lg_u64 vcc, 0
	s_cselect_b64 s[26:27], -1, 0
	s_cbranch_vccnz .Lu0_12

.Lu1_1:
	ds_read_b64_tr_b16 v[178:179], v206 offset:40960
	ds_read_b64_tr_b16 v[180:181], v206 offset:41984
	s_waitcnt lgkmcnt(9)
	v_mfma_f32_32x32x16_f16 v[98:113], v[82:85], v[154:157], v[34:49]
	v_add_f32_e32 v224, v66, v68
	v_add_f32_e32 v225, v67, v69
	v_add_f32_e32 v224, v70, v224
	v_add_f32_e32 v225, v71, v225
	v_cvt_pk_f16_f32 v158, v66, v67
	v_cvt_pk_f16_f32 v159, v68, v69
	ds_read_b64_tr_b16 v[174:175], v207 offset:40960
	ds_read_b64_tr_b16 v[176:177], v207 offset:41984
	s_waitcnt lgkmcnt(10)
	v_mfma_f32_32x32x16_f16 v[82:97], v[170:173], v[154:157], v[34:49]
	v_add_f32_e32 v224, v72, v224
	v_add_f32_e32 v225, v73, v225
	v_add_f32_e32 v224, v74, v224
	v_add_f32_e32 v225, v75, v225
	v_cvt_pk_f16_f32 v160, v70, v71
	v_cvt_pk_f16_f32 v161, v72, v73
	ds_read_b64_tr_b16 v[170:171], v206 offset:43008
	ds_read_b64_tr_b16 v[172:173], v206 offset:44032
	s_waitcnt lgkmcnt(11)
	v_mfma_f32_32x32x16_f16 v[98:113], v[166:169], v[146:149], v[98:113]
	v_add_f32_e32 v224, v76, v224
	v_add_f32_e32 v225, v77, v225
	v_add_f32_e32 v224, v78, v224
	v_add_f32_e32 v225, v79, v225
	v_cvt_pk_f16_f32 v150, v74, v75
	v_cvt_pk_f16_f32 v151, v76, v77
	ds_read_b64_tr_b16 v[74:75], v207 offset:43008
	ds_read_b64_tr_b16 v[76:77], v207 offset:44032
	s_waitcnt lgkmcnt(12)
	v_mfma_f32_32x32x16_f16 v[82:97], v[162:165], v[146:149], v[82:97]
	v_add_f32_e32 v224, v80, v224
	v_add_f32_e32 v225, v81, v225
	v_add_f32_e32 v224, v50, v224
	v_add_f32_e32 v225, v51, v225
	v_cvt_pk_f16_f32 v152, v78, v79
	v_cvt_pk_f16_f32 v153, v80, v81
	ds_read_b64_tr_b16 v[70:71], v206 offset:45056
	ds_read_b64_tr_b16 v[72:73], v206 offset:46080
	s_waitcnt lgkmcnt(13)
	v_mfma_f32_32x32x16_f16 v[98:113], v[126:129], v[138:141], v[98:113]
	v_add_f32_e32 v224, v52, v224
	v_add_f32_e32 v225, v53, v225
	v_add_f32_e32 v224, v54, v224
	v_add_f32_e32 v225, v55, v225
	v_cvt_pk_f16_f32 v142, v50, v51
	v_cvt_pk_f16_f32 v143, v52, v53
	ds_read_b64_tr_b16 v[66:67], v207 offset:45056
	ds_read_b64_tr_b16 v[68:69], v207 offset:46080
	s_waitcnt lgkmcnt(14)
	v_mfma_f32_32x32x16_f16 v[82:97], v[122:125], v[138:141], v[82:97]
	v_add_f32_e32 v224, v56, v224
	v_add_f32_e32 v225, v57, v225
	v_add_f32_e32 v224, v58, v224
	v_add_f32_e32 v225, v59, v225
	v_cvt_pk_f16_f32 v144, v54, v55
	v_cvt_pk_f16_f32 v145, v56, v57
	ds_read_b64_tr_b16 v[54:55], v206 offset:47104
	ds_read_b64_tr_b16 v[56:57], v206 offset:48128
	s_waitcnt lgkmcnt(14)
	v_mfma_f32_32x32x16_f16 v[98:113], v[118:121], v[134:137], v[98:113]
	v_add_f32_e32 v224, v60, v224
	v_add_f32_e32 v225, v61, v225
	v_add_f32_e32 v224, v62, v224
	v_add_f32_e32 v225, v63, v225
	v_cvt_pk_f16_f32 v130, v58, v59
	v_cvt_pk_f16_f32 v131, v60, v61
	ds_read_b64_tr_b16 v[50:51], v207 offset:47104
	ds_read_b64_tr_b16 v[52:53], v207 offset:48128
	v_mfma_f32_32x32x16_f16 v[82:97], v[114:117], v[134:137], v[82:97]
	v_add_f32_e32 v224, v64, v224
	v_add_f32_e32 v225, v65, v225
	v_add_f32_e32 v60, v224, v225
	v_cvt_pk_f16_f32 v132, v62, v63
	v_cvt_pk_f16_f32 v133, v64, v65
	s_add_i32 s26, s42, s36
	s_mov_b32 m0, s26
	s_nop 0
	global_load_lds_dwordx4 v221, s[50:51]
	s_add_i32 s26, s39, s35
	s_mov_b32 m0, s26
	s_nop 0
	global_load_lds_dwordx4 v222, s[52:53]
	v_max_f32_e32 v58, v98, v99
	v_max3_f32 v59, v100, v101, v83
	v_max3_f32 v58, v58, v82, v84
	v_max3_f32 v58, v58, v85, v102
	v_max3_f32 v59, v59, v104, v105
	v_max3_f32 v58, v58, v103, v86
	v_max3_f32 v59, v59, v88, v89
	v_max3_f32 v58, v58, v87, v106
	v_max3_f32 v59, v59, v108, v109
	v_max3_f32 v58, v58, v107, v90
	v_max3_f32 v59, v59, v92, v93
	v_max3_f32 v58, v58, v91, v110
	v_max3_f32 v59, v59, v112, v113
	v_max3_f32 v58, v58, v111, v94
	v_max3_f32 v59, v59, v96, v97
	v_max3_f32 v58, v58, v95, v59
	v_add_f32_e32 v198, v183, v60
	v_cmp_lt_f32_e32 vcc, s41, v58
	s_cmp_lg_u64 vcc, 0
	s_cselect_b64 s[26:27], -1, 0
	s_cbranch_vccnz .Lu1_9

.Lu1_4:
	s_add_i32 s26, s39, 0x2000
	s_cmpk_lg_i32 s39, 0x4000
	s_cselect_b32 s43, s26, 0
	ds_read_b64_tr_b16 v[126:127], v206 offset:24576
	ds_read_b64_tr_b16 v[128:129], v206 offset:25600
	s_waitcnt lgkmcnt(9)
	v_mfma_f32_32x32x16_f16 v[66:81], v[58:61], v[154:157], v[34:49]
	v_add_f32_e32 v224, v98, v100
	v_add_f32_e32 v225, v99, v101
	v_add_f32_e32 v224, v102, v224
	v_add_f32_e32 v225, v103, v225
	v_cvt_pk_f16_f32 v158, v98, v99
	v_cvt_pk_f16_f32 v159, v100, v101
	ds_read_b64_tr_b16 v[122:123], v207 offset:24576
	ds_read_b64_tr_b16 v[124:125], v207 offset:25600
	s_waitcnt lgkmcnt(10)
	v_mfma_f32_32x32x16_f16 v[50:65], v[114:117], v[154:157], v[34:49]
	v_add_f32_e32 v224, v104, v224
	v_add_f32_e32 v225, v105, v225
	v_add_f32_e32 v224, v106, v224
	v_add_f32_e32 v225, v107, v225
	v_cvt_pk_f16_f32 v160, v102, v103
	v_cvt_pk_f16_f32 v161, v104, v105
	ds_read_b64_tr_b16 v[118:119], v206 offset:26624
	ds_read_b64_tr_b16 v[120:121], v206 offset:27648
	s_waitcnt lgkmcnt(11)
	v_mfma_f32_32x32x16_f16 v[66:81], v[182:185], v[146:149], v[66:81]
	v_add_f32_e32 v224, v108, v224
	v_add_f32_e32 v225, v109, v225
	v_add_f32_e32 v224, v110, v224
	v_add_f32_e32 v225, v111, v225
	v_cvt_pk_f16_f32 v150, v106, v107
	v_cvt_pk_f16_f32 v151, v108, v109
	ds_read_b64_tr_b16 v[114:115], v207 offset:26624
	ds_read_b64_tr_b16 v[116:117], v207 offset:27648
	s_waitcnt lgkmcnt(12)
	v_mfma_f32_32x32x16_f16 v[50:65], v[174:177], v[146:149], v[50:65]
	v_add_f32_e32 v224, v112, v224
	v_add_f32_e32 v225, v113, v225
	v_add_f32_e32 v224, v82, v224
	v_add_f32_e32 v225, v83, v225
	v_cvt_pk_f16_f32 v152, v110, v111
	v_cvt_pk_f16_f32 v153, v112, v113
	ds_read_b64_tr_b16 v[106:107], v206 offset:28672
	ds_read_b64_tr_b16 v[108:109], v206 offset:29696
	s_waitcnt lgkmcnt(13)
	v_mfma_f32_32x32x16_f16 v[66:81], v[178:181], v[138:141], v[66:81]
	v_add_f32_e32 v224, v84, v224
	v_add_f32_e32 v225, v85, v225
	v_add_f32_e32 v224, v86, v224
	v_add_f32_e32 v225, v87, v225
	v_cvt_pk_f16_f32 v142, v82, v83
	v_cvt_pk_f16_f32 v143, v84, v85
	ds_read_b64_tr_b16 v[102:103], v207 offset:28672
	ds_read_b64_tr_b16 v[104:105], v207 offset:29696
	s_waitcnt lgkmcnt(14)
	v_mfma_f32_32x32x16_f16 v[50:65], v[166:169], v[138:141], v[50:65]
	v_add_f32_e32 v224, v88, v224
	v_add_f32_e32 v225, v89, v225
	v_add_f32_e32 v224, v90, v224
	v_add_f32_e32 v225, v91, v225
	v_cvt_pk_f16_f32 v144, v86, v87
	v_cvt_pk_f16_f32 v145, v88, v89
	ds_read_b64_tr_b16 v[98:99], v206 offset:30720
	ds_read_b64_tr_b16 v[100:101], v206 offset:31744
	s_waitcnt lgkmcnt(14)
	v_mfma_f32_32x32x16_f16 v[66:81], v[170:173], v[134:137], v[66:81]
	v_add_f32_e32 v224, v92, v224
	v_add_f32_e32 v225, v93, v225
	v_add_f32_e32 v224, v94, v224
	v_add_f32_e32 v225, v95, v225
	v_cvt_pk_f16_f32 v130, v90, v91
	v_cvt_pk_f16_f32 v131, v92, v93
	ds_read_b64_tr_b16 v[86:87], v207 offset:30720
	ds_read_b64_tr_b16 v[88:89], v207 offset:31744
	v_mfma_f32_32x32x16_f16 v[50:65], v[162:165], v[134:137], v[50:65]
	v_add_f32_e32 v224, v96, v224
	v_add_f32_e32 v225, v97, v225
	v_add_f32_e32 v84, v224, v225
	v_cvt_pk_f16_f32 v132, v94, v95
	v_cvt_pk_f16_f32 v133, v96, v97
	s_add_u32 s54, s50, 0x2000
	s_addc_u32 s55, s51, 0
	s_add_i32 s26, s39, s36
	s_mov_b32 m0, s26
	s_nop 0
	global_load_lds_dwordx4 v221, s[54:55]
	v_max_f32_e32 v82, v66, v67
	s_nop 1
	v_max3_f32 v83, v68, v69, v51
	v_max3_f32 v82, v82, v50, v52
	v_max3_f32 v82, v82, v53, v70
	v_max3_f32 v83, v83, v72, v73
	v_max3_f32 v82, v82, v71, v54
	v_max3_f32 v83, v83, v56, v57
	v_max3_f32 v82, v82, v55, v74
	v_max3_f32 v83, v83, v76, v77
	v_max3_f32 v82, v82, v75, v58
	v_max3_f32 v83, v83, v60, v61
	v_max3_f32 v82, v82, v59, v78
	v_max3_f32 v83, v83, v80, v81
	v_max3_f32 v82, v82, v79, v62
	v_max3_f32 v83, v83, v64, v65
	v_max3_f32 v82, v82, v63, v83
	v_add_f32_e32 v183, v198, v84
	s_add_u32 s54, s52, 0x2000
	s_addc_u32 s55, s53, 0
	s_add_i32 s26, s43, s35
	s_mov_b32 m0, s26
	s_nop 0
	global_load_lds_dwordx4 v222, s[54:55]
	v_cmp_lt_f32_e32 vcc, s41, v82
	s_cmp_lg_u64 vcc, 0
	s_cselect_b64 s[26:27], -1, 0
	s_cbranch_vccnz .Lu1_12

.Lu2_1:
	ds_read_b64_tr_b16 v[178:179], v206 offset:32768
	ds_read_b64_tr_b16 v[180:181], v206 offset:33792
	s_waitcnt lgkmcnt(9)
	v_mfma_f32_32x32x16_f16 v[98:113], v[82:85], v[154:157], v[34:49]
	v_add_f32_e32 v224, v66, v68
	v_add_f32_e32 v225, v67, v69
	v_add_f32_e32 v224, v70, v224
	v_add_f32_e32 v225, v71, v225
	v_cvt_pk_f16_f32 v158, v66, v67
	v_cvt_pk_f16_f32 v159, v68, v69
	ds_read_b64_tr_b16 v[174:175], v207 offset:32768
	ds_read_b64_tr_b16 v[176:177], v207 offset:33792
	s_waitcnt lgkmcnt(10)
	v_mfma_f32_32x32x16_f16 v[82:97], v[170:173], v[154:157], v[34:49]
	v_add_f32_e32 v224, v72, v224
	v_add_f32_e32 v225, v73, v225
	v_add_f32_e32 v224, v74, v224
	v_add_f32_e32 v225, v75, v225
	v_cvt_pk_f16_f32 v160, v70, v71
	v_cvt_pk_f16_f32 v161, v72, v73
	ds_read_b64_tr_b16 v[170:171], v206 offset:34816
	ds_read_b64_tr_b16 v[172:173], v206 offset:35840
	s_waitcnt lgkmcnt(11)
	v_mfma_f32_32x32x16_f16 v[98:113], v[166:169], v[146:149], v[98:113]
	v_add_f32_e32 v224, v76, v224
	v_add_f32_e32 v225, v77, v225
	v_add_f32_e32 v224, v78, v224
	v_add_f32_e32 v225, v79, v225
	v_cvt_pk_f16_f32 v150, v74, v75
	v_cvt_pk_f16_f32 v151, v76, v77
	ds_read_b64_tr_b16 v[74:75], v207 offset:34816
	ds_read_b64_tr_b16 v[76:77], v207 offset:35840
	s_waitcnt lgkmcnt(12)
	v_mfma_f32_32x32x16_f16 v[82:97], v[162:165], v[146:149], v[82:97]
	v_add_f32_e32 v224, v80, v224
	v_add_f32_e32 v225, v81, v225
	v_add_f32_e32 v224, v50, v224
	v_add_f32_e32 v225, v51, v225
	v_cvt_pk_f16_f32 v152, v78, v79
	v_cvt_pk_f16_f32 v153, v80, v81
	ds_read_b64_tr_b16 v[70:71], v206 offset:36864
	ds_read_b64_tr_b16 v[72:73], v206 offset:37888
	s_waitcnt lgkmcnt(13)
	v_mfma_f32_32x32x16_f16 v[98:113], v[126:129], v[138:141], v[98:113]
	v_add_f32_e32 v224, v52, v224
	v_add_f32_e32 v225, v53, v225
	v_add_f32_e32 v224, v54, v224
	v_add_f32_e32 v225, v55, v225
	v_cvt_pk_f16_f32 v142, v50, v51
	v_cvt_pk_f16_f32 v143, v52, v53
	ds_read_b64_tr_b16 v[66:67], v207 offset:36864
	ds_read_b64_tr_b16 v[68:69], v207 offset:37888
	s_waitcnt lgkmcnt(14)
	v_mfma_f32_32x32x16_f16 v[82:97], v[122:125], v[138:141], v[82:97]
	v_add_f32_e32 v224, v56, v224
	v_add_f32_e32 v225, v57, v225
	v_add_f32_e32 v224, v58, v224
	v_add_f32_e32 v225, v59, v225
	v_cvt_pk_f16_f32 v144, v54, v55
	v_cvt_pk_f16_f32 v145, v56, v57
	ds_read_b64_tr_b16 v[54:55], v206 offset:38912
	ds_read_b64_tr_b16 v[56:57], v206 offset:39936
	s_waitcnt lgkmcnt(14)
	v_mfma_f32_32x32x16_f16 v[98:113], v[118:121], v[134:137], v[98:113]
	v_add_f32_e32 v224, v60, v224
	v_add_f32_e32 v225, v61, v225
	v_add_f32_e32 v224, v62, v224
	v_add_f32_e32 v225, v63, v225
	v_cvt_pk_f16_f32 v130, v58, v59
	v_cvt_pk_f16_f32 v131, v60, v61
	ds_read_b64_tr_b16 v[50:51], v207 offset:38912
	ds_read_b64_tr_b16 v[52:53], v207 offset:39936
	v_mfma_f32_32x32x16_f16 v[82:97], v[114:117], v[134:137], v[82:97]
	v_add_f32_e32 v224, v64, v224
	v_add_f32_e32 v225, v65, v225
	v_add_f32_e32 v60, v224, v225
	v_cvt_pk_f16_f32 v132, v62, v63
	v_cvt_pk_f16_f32 v133, v64, v65
	s_add_i32 s26, s42, s36
	s_mov_b32 m0, s26
	s_nop 0
	global_load_lds_dwordx4 v221, s[50:51]
	s_add_i32 s26, s39, s35
	s_mov_b32 m0, s26
	s_nop 0
	global_load_lds_dwordx4 v222, s[52:53]
	v_max_f32_e32 v58, v98, v99
	v_max3_f32 v59, v100, v101, v83
	v_max3_f32 v58, v58, v82, v84
	v_max3_f32 v58, v58, v85, v102
	v_max3_f32 v59, v59, v104, v105
	v_max3_f32 v58, v58, v103, v86
	v_max3_f32 v59, v59, v88, v89
	v_max3_f32 v58, v58, v87, v106
	v_max3_f32 v59, v59, v108, v109
	v_max3_f32 v58, v58, v107, v90
	v_max3_f32 v59, v59, v92, v93
	v_max3_f32 v58, v58, v91, v110
	v_max3_f32 v59, v59, v112, v113
	v_max3_f32 v58, v58, v111, v94
	v_max3_f32 v59, v59, v96, v97
	v_max3_f32 v58, v58, v95, v59
	v_add_f32_e32 v198, v183, v60
	v_cmp_lt_f32_e32 vcc, s41, v58
	s_cmp_lg_u64 vcc, 0
	s_cselect_b64 s[26:27], -1, 0
	s_cbranch_vccnz .Lu2_9

.Lu2_4:
	s_add_i32 s26, s39, 0x2000
	s_cmpk_lg_i32 s39, 0x4000
	s_cselect_b32 s43, s26, 0
	ds_read_b64_tr_b16 v[126:127], v206 offset:40960
	ds_read_b64_tr_b16 v[128:129], v206 offset:41984
	s_waitcnt lgkmcnt(9)
	v_mfma_f32_32x32x16_f16 v[66:81], v[58:61], v[154:157], v[34:49]
	v_add_f32_e32 v224, v98, v100
	v_add_f32_e32 v225, v99, v101
	v_add_f32_e32 v224, v102, v224
	v_add_f32_e32 v225, v103, v225
	v_cvt_pk_f16_f32 v158, v98, v99
	v_cvt_pk_f16_f32 v159, v100, v101
	ds_read_b64_tr_b16 v[122:123], v207 offset:40960
	ds_read_b64_tr_b16 v[124:125], v207 offset:41984
	s_waitcnt lgkmcnt(10)
	v_mfma_f32_32x32x16_f16 v[50:65], v[114:117], v[154:157], v[34:49]
	v_add_f32_e32 v224, v104, v224
	v_add_f32_e32 v225, v105, v225
	v_add_f32_e32 v224, v106, v224
	v_add_f32_e32 v225, v107, v225
	v_cvt_pk_f16_f32 v160, v102, v103
	v_cvt_pk_f16_f32 v161, v104, v105
	ds_read_b64_tr_b16 v[118:119], v206 offset:43008
	ds_read_b64_tr_b16 v[120:121], v206 offset:44032
	s_waitcnt lgkmcnt(11)
	v_mfma_f32_32x32x16_f16 v[66:81], v[182:185], v[146:149], v[66:81]
	v_add_f32_e32 v224, v108, v224
	v_add_f32_e32 v225, v109, v225
	v_add_f32_e32 v224, v110, v224
	v_add_f32_e32 v225, v111, v225
	v_cvt_pk_f16_f32 v150, v106, v107
	v_cvt_pk_f16_f32 v151, v108, v109
	ds_read_b64_tr_b16 v[114:115], v207 offset:43008
	ds_read_b64_tr_b16 v[116:117], v207 offset:44032
	s_waitcnt lgkmcnt(12)
	v_mfma_f32_32x32x16_f16 v[50:65], v[174:177], v[146:149], v[50:65]
	v_add_f32_e32 v224, v112, v224
	v_add_f32_e32 v225, v113, v225
	v_add_f32_e32 v224, v82, v224
	v_add_f32_e32 v225, v83, v225
	v_cvt_pk_f16_f32 v152, v110, v111
	v_cvt_pk_f16_f32 v153, v112, v113
	ds_read_b64_tr_b16 v[106:107], v206 offset:45056
	ds_read_b64_tr_b16 v[108:109], v206 offset:46080
	s_waitcnt lgkmcnt(13)
	v_mfma_f32_32x32x16_f16 v[66:81], v[178:181], v[138:141], v[66:81]
	v_add_f32_e32 v224, v84, v224
	v_add_f32_e32 v225, v85, v225
	v_add_f32_e32 v224, v86, v224
	v_add_f32_e32 v225, v87, v225
	v_cvt_pk_f16_f32 v142, v82, v83
	v_cvt_pk_f16_f32 v143, v84, v85
	ds_read_b64_tr_b16 v[102:103], v207 offset:45056
	ds_read_b64_tr_b16 v[104:105], v207 offset:46080
	s_waitcnt lgkmcnt(14)
	v_mfma_f32_32x32x16_f16 v[50:65], v[166:169], v[138:141], v[50:65]
	v_add_f32_e32 v224, v88, v224
	v_add_f32_e32 v225, v89, v225
	v_add_f32_e32 v224, v90, v224
	v_add_f32_e32 v225, v91, v225
	v_cvt_pk_f16_f32 v144, v86, v87
	v_cvt_pk_f16_f32 v145, v88, v89
	ds_read_b64_tr_b16 v[98:99], v206 offset:47104
	ds_read_b64_tr_b16 v[100:101], v206 offset:48128
	s_waitcnt lgkmcnt(14)
	v_mfma_f32_32x32x16_f16 v[66:81], v[170:173], v[134:137], v[66:81]
	v_add_f32_e32 v224, v92, v224
	v_add_f32_e32 v225, v93, v225
	v_add_f32_e32 v224, v94, v224
	v_add_f32_e32 v225, v95, v225
	v_cvt_pk_f16_f32 v130, v90, v91
	v_cvt_pk_f16_f32 v131, v92, v93
	ds_read_b64_tr_b16 v[86:87], v207 offset:47104
	ds_read_b64_tr_b16 v[88:89], v207 offset:48128
	v_mfma_f32_32x32x16_f16 v[50:65], v[162:165], v[134:137], v[50:65]
	v_add_f32_e32 v224, v96, v224
	v_add_f32_e32 v225, v97, v225
	v_add_f32_e32 v84, v224, v225
	v_cvt_pk_f16_f32 v132, v94, v95
	v_cvt_pk_f16_f32 v133, v96, v97
	s_add_u32 s54, s50, 0x2000
	s_addc_u32 s55, s51, 0
	s_add_i32 s26, s39, s36
	s_mov_b32 m0, s26
	s_nop 0
	global_load_lds_dwordx4 v221, s[54:55]
	v_max_f32_e32 v82, v66, v67
	s_nop 1
	v_max3_f32 v83, v68, v69, v51
	v_max3_f32 v82, v82, v50, v52
	v_max3_f32 v82, v82, v53, v70
	v_max3_f32 v83, v83, v72, v73
	v_max3_f32 v82, v82, v71, v54
	v_max3_f32 v83, v83, v56, v57
	v_max3_f32 v82, v82, v55, v74
	v_max3_f32 v83, v83, v76, v77
	v_max3_f32 v82, v82, v75, v58
	v_max3_f32 v83, v83, v60, v61
	v_max3_f32 v82, v82, v59, v78
	v_max3_f32 v83, v83, v80, v81
	v_max3_f32 v82, v82, v79, v62
	v_max3_f32 v83, v83, v64, v65
	v_max3_f32 v82, v82, v63, v83
	v_add_f32_e32 v183, v198, v84
	s_add_u32 s54, s52, 0x2000
	s_addc_u32 s55, s53, 0
	s_add_i32 s26, s43, s35
	s_mov_b32 m0, s26
	s_nop 0
	global_load_lds_dwordx4 v222, s[54:55]
	v_cmp_lt_f32_e32 vcc, s41, v82
	s_cmp_lg_u64 vcc, 0
	s_cselect_b64 s[26:27], -1, 0
	s_cbranch_vccnz .Lu2_12

	.amdhsa_kernel _ZN4attn8attn_fwdEPKDF16_PDF16_
		.amdhsa_group_segment_fixed_size 83968
		.amdhsa_private_segment_fixed_size 0
		.amdhsa_kernarg_size 16
		.amdhsa_user_sgpr_count 2
		.amdhsa_user_sgpr_dispatch_ptr 0
		.amdhsa_user_sgpr_queue_ptr 0
		.amdhsa_user_sgpr_kernarg_segment_ptr 1
		.amdhsa_user_sgpr_dispatch_id 0
		.amdhsa_user_sgpr_kernarg_preload_length 0
		.amdhsa_user_sgpr_kernarg_preload_offset 0
		.amdhsa_user_sgpr_private_segment_size 0
		.amdhsa_uses_dynamic_stack 0
		.amdhsa_enable_private_segment 0
		.amdhsa_system_sgpr_workgroup_id_x 1
		.amdhsa_system_sgpr_workgroup_id_y 0
		.amdhsa_system_sgpr_workgroup_id_z 0
		.amdhsa_system_sgpr_workgroup_info 0
		.amdhsa_system_vgpr_workitem_id 0
		.amdhsa_next_free_vgpr 228
		.amdhsa_next_free_sgpr 96
		.amdhsa_accum_offset 228
		.amdhsa_reserve_vcc 1
		.amdhsa_float_round_mode_32 0
		.amdhsa_float_round_mode_16_64 0
		.amdhsa_float_denorm_mode_32 3
		.amdhsa_float_denorm_mode_16_64 3
		.amdhsa_dx10_clamp 1
		.amdhsa_ieee_mode 1
		.amdhsa_fp16_overflow 0
		.amdhsa_tg_split 0
		.amdhsa_exception_fp_ieee_invalid_op 0
		.amdhsa_exception_fp_denorm_src 0
		.amdhsa_exception_fp_ieee_div_zero 0
		.amdhsa_exception_fp_ieee_overflow 0
		.amdhsa_exception_fp_ieee_underflow 0
		.amdhsa_exception_fp_ieee_inexact 0
		.amdhsa_exception_int_div_zero 0
	.end_amdhsa_kernel
